# speedup vs baseline: 1.0034x; 1.0034x over previous
_Z4k_lnPKfS0_S0_PDF16_PfS2_7CvtArgs:
	s_cmpk_lt_u32 s2, 0x100
	s_mov_b64 s[4:5], -1
	s_cbranch_scc0 .LBB0_8
	s_load_dwordx8 s[4:11], s[0:1], 0x0
	s_load_dwordx4 s[12:15], s[0:1], 0x20
	s_lshr_b32 s16, s2, 7
	s_lshl_b32 s3, s2, 5
	s_mov_b32 s17, 0
	s_and_b32 s3, s3, 0xfe0
	s_lshl_b64 s[18:19], s[16:17], 23
	v_and_b32_e32 v8, 0x1e0, v0
	s_waitcnt lgkmcnt(0)
	s_add_u32 s4, s4, s18
	s_addc_u32 s5, s5, s19
	v_lshlrev_b32_e32 v4, 14, v8
	v_mov_b32_e32 v5, 0
	v_and_b32_e32 v1, 31, v0
	v_lshl_add_u64 v[2:3], s[4:5], 0, v[4:5]
	s_lshl_b32 s4, s3, 2
	s_mov_b32 s5, s17
	v_lshl_add_u64 v[2:3], v[2:3], 0, s[4:5]
	v_lshlrev_b32_e32 v4, 2, v1
	v_lshl_add_u64 v[2:3], v[2:3], 0, v[4:5]
	s_mov_b64 s[4:5], 0
	v_mov_b32_e32 v6, v5
	v_mov_b32_e32 v7, v5
	v_lshl_add_u64 v[10:11], v[2:3], 0, s[4:5]
	v_add_co_u32_e32 v14, vcc, 0x4000, v10
	global_load_dword v12, v[10:11], off
	s_nop 0
	v_addc_co_u32_e32 v15, vcc, 0, v11, vcc
	v_add_co_u32_e32 v16, vcc, 0x8000, v10
	global_load_dword v14, v[14:15], off
	s_nop 0
	v_addc_co_u32_e32 v17, vcc, 0, v11, vcc
	v_add_co_u32_e32 v18, vcc, 0xc000, v10
	s_add_u32 s4, s4, 0x40000
	s_nop 0
	v_addc_co_u32_e32 v19, vcc, 0, v11, vcc
	v_add_co_u32_e32 v20, vcc, 0x10000, v10
	global_load_dword v22, v[16:17], off
	global_load_dword v24, v[18:19], off
	v_addc_co_u32_e32 v21, vcc, 0, v11, vcc
	v_add_co_u32_e32 v16, vcc, 0x14000, v10
	s_addc_u32 s5, s5, 0
	s_nop 0
	v_addc_co_u32_e32 v17, vcc, 0, v11, vcc
	v_add_co_u32_e32 v18, vcc, 0x18000, v10
	global_load_dword v26, v[20:21], off
	global_load_dword v28, v[16:17], off
	v_addc_co_u32_e32 v19, vcc, 0, v11, vcc
	v_add_co_u32_e32 v16, vcc, 0x1c000, v10
	s_nop 0
	v_addc_co_u32_e32 v17, vcc, 0, v11, vcc
	v_add_co_u32_e32 v20, vcc, 0x20000, v10
	global_load_dword v30, v[18:19], off
	global_load_dword v32, v[16:17], off
	v_addc_co_u32_e32 v21, vcc, 0, v11, vcc
	v_add_co_u32_e32 v16, vcc, 0x24000, v10
	global_load_dword v18, v[20:21], off
	s_nop 0
	v_addc_co_u32_e32 v17, vcc, 0, v11, vcc
	v_add_co_u32_e32 v20, vcc, 0x28000, v10
	v_addc_co_u32_e32 v21, vcc, 0, v11, vcc
	v_add_co_u32_e32 v34, vcc, 0x2c000, v10
	global_load_dword v36, v[16:17], off
	global_load_dword v38, v[20:21], off
	v_addc_co_u32_e32 v35, vcc, 0, v11, vcc
	v_add_co_u32_e32 v16, vcc, 0x30000, v10
	s_nop 0
	v_addc_co_u32_e32 v17, vcc, 0, v11, vcc
	v_add_co_u32_e32 v20, vcc, 0x34000, v10
	global_load_dword v40, v[34:35], off
	global_load_dword v42, v[16:17], off
	v_addc_co_u32_e32 v21, vcc, 0, v11, vcc
	v_add_co_u32_e32 v16, vcc, 0x38000, v10
	v_addc_co_u32_e32 v17, vcc, 0, v11, vcc
	v_add_co_u32_e32 v10, vcc, 0x3c000, v10
	global_load_dword v34, v[20:21], off
	global_load_dword v44, v[16:17], off
	v_addc_co_u32_e32 v11, vcc, 0, v11, vcc
	global_load_dword v10, v[10:11], off
	v_lshl_add_u64 v[66:67], v[2:3], 0, s[4:5]
	v_add_co_u32_e32 v70, vcc, 0x4000, v66
	global_load_dword v68, v[66:67], off
	s_nop 0
	v_addc_co_u32_e32 v71, vcc, 0, v67, vcc
	v_add_co_u32_e32 v72, vcc, 0x8000, v66
	global_load_dword v70, v[70:71], off
	s_nop 0
	v_addc_co_u32_e32 v73, vcc, 0, v67, vcc
	v_add_co_u32_e32 v74, vcc, 0xc000, v66
	s_add_u32 s4, s4, 0x40000
	s_nop 0
	v_addc_co_u32_e32 v75, vcc, 0, v67, vcc
	v_add_co_u32_e32 v76, vcc, 0x10000, v66
	global_load_dword v78, v[72:73], off
	global_load_dword v80, v[74:75], off
	v_addc_co_u32_e32 v77, vcc, 0, v67, vcc
	v_add_co_u32_e32 v72, vcc, 0x14000, v66
	s_addc_u32 s5, s5, 0
	s_nop 0
	v_addc_co_u32_e32 v73, vcc, 0, v67, vcc
	v_add_co_u32_e32 v74, vcc, 0x18000, v66
	global_load_dword v82, v[76:77], off
	global_load_dword v84, v[72:73], off
	v_addc_co_u32_e32 v75, vcc, 0, v67, vcc
	v_add_co_u32_e32 v72, vcc, 0x1c000, v66
	s_nop 0
	v_addc_co_u32_e32 v73, vcc, 0, v67, vcc
	v_add_co_u32_e32 v76, vcc, 0x20000, v66
	global_load_dword v86, v[74:75], off
	global_load_dword v88, v[72:73], off
	v_addc_co_u32_e32 v77, vcc, 0, v67, vcc
	v_add_co_u32_e32 v72, vcc, 0x24000, v66
	global_load_dword v74, v[76:77], off
	s_nop 0
	v_addc_co_u32_e32 v73, vcc, 0, v67, vcc
	v_add_co_u32_e32 v76, vcc, 0x28000, v66
	v_addc_co_u32_e32 v77, vcc, 0, v67, vcc
	v_add_co_u32_e32 v90, vcc, 0x2c000, v66
	global_load_dword v92, v[72:73], off
	global_load_dword v94, v[76:77], off
	v_addc_co_u32_e32 v91, vcc, 0, v67, vcc
	v_add_co_u32_e32 v72, vcc, 0x30000, v66
	s_nop 0
	v_addc_co_u32_e32 v73, vcc, 0, v67, vcc
	v_add_co_u32_e32 v76, vcc, 0x34000, v66
	global_load_dword v96, v[90:91], off
	global_load_dword v98, v[72:73], off
	v_addc_co_u32_e32 v77, vcc, 0, v67, vcc
	v_add_co_u32_e32 v72, vcc, 0x38000, v66
	v_addc_co_u32_e32 v73, vcc, 0, v67, vcc
	v_add_co_u32_e32 v66, vcc, 0x3c000, v66
	global_load_dword v90, v[76:77], off
	global_load_dword v100, v[72:73], off
	v_addc_co_u32_e32 v67, vcc, 0, v67, vcc
	global_load_dword v66, v[66:67], off
	s_waitcnt vmcnt(31)
	v_mul_f32_e32 v13, v12, v12
	v_pk_add_f32 v[6:7], v[6:7], v[12:13]
	s_waitcnt vmcnt(30)
	v_mul_f32_e32 v15, v14, v14
	v_pk_add_f32 v[6:7], v[6:7], v[14:15]
	s_waitcnt vmcnt(29)
	v_mul_f32_e32 v23, v22, v22
	v_pk_add_f32 v[6:7], v[6:7], v[22:23]
	s_waitcnt vmcnt(28)
	v_mul_f32_e32 v25, v24, v24
	v_pk_add_f32 v[6:7], v[6:7], v[24:25]
	s_waitcnt vmcnt(27)
	v_mul_f32_e32 v27, v26, v26
	v_pk_add_f32 v[6:7], v[6:7], v[26:27]
	s_waitcnt vmcnt(26)
	v_mul_f32_e32 v29, v28, v28
	v_pk_add_f32 v[6:7], v[6:7], v[28:29]
	s_waitcnt vmcnt(25)
	v_mul_f32_e32 v31, v30, v30
	v_pk_add_f32 v[6:7], v[6:7], v[30:31]
	s_waitcnt vmcnt(24)
	v_mul_f32_e32 v33, v32, v32
	v_pk_add_f32 v[6:7], v[6:7], v[32:33]
	s_waitcnt vmcnt(23)
	v_mul_f32_e32 v19, v18, v18
	v_pk_add_f32 v[6:7], v[6:7], v[18:19]
	s_waitcnt vmcnt(22)
	v_mul_f32_e32 v37, v36, v36
	v_pk_add_f32 v[6:7], v[6:7], v[36:37]
	s_waitcnt vmcnt(21)
	v_mul_f32_e32 v39, v38, v38
	v_pk_add_f32 v[6:7], v[6:7], v[38:39]
	s_waitcnt vmcnt(20)
	v_mul_f32_e32 v41, v40, v40
	v_pk_add_f32 v[6:7], v[6:7], v[40:41]
	s_waitcnt vmcnt(19)
	v_mul_f32_e32 v43, v42, v42
	v_pk_add_f32 v[6:7], v[6:7], v[42:43]
	s_waitcnt vmcnt(18)
	v_mul_f32_e32 v35, v34, v34
	v_pk_add_f32 v[6:7], v[6:7], v[34:35]
	s_waitcnt vmcnt(17)
	v_mul_f32_e32 v45, v44, v44
	v_pk_add_f32 v[6:7], v[6:7], v[44:45]
	s_waitcnt vmcnt(16)
	v_mul_f32_e32 v11, v10, v10
	v_pk_add_f32 v[6:7], v[6:7], v[10:11]
	s_waitcnt vmcnt(15)
	v_mul_f32_e32 v69, v68, v68
	v_pk_add_f32 v[6:7], v[6:7], v[68:69]
	s_waitcnt vmcnt(14)
	v_mul_f32_e32 v71, v70, v70
	v_pk_add_f32 v[6:7], v[6:7], v[70:71]
	s_waitcnt vmcnt(13)
	v_mul_f32_e32 v79, v78, v78
	v_pk_add_f32 v[6:7], v[6:7], v[78:79]
	s_waitcnt vmcnt(12)
	v_mul_f32_e32 v81, v80, v80
	v_pk_add_f32 v[6:7], v[6:7], v[80:81]
	s_waitcnt vmcnt(11)
	v_mul_f32_e32 v83, v82, v82
	v_pk_add_f32 v[6:7], v[6:7], v[82:83]
	s_waitcnt vmcnt(10)
	v_mul_f32_e32 v85, v84, v84
	v_pk_add_f32 v[6:7], v[6:7], v[84:85]
	s_waitcnt vmcnt(9)
	v_mul_f32_e32 v87, v86, v86
	v_pk_add_f32 v[6:7], v[6:7], v[86:87]
	s_waitcnt vmcnt(8)
	v_mul_f32_e32 v89, v88, v88
	v_pk_add_f32 v[6:7], v[6:7], v[88:89]
	s_waitcnt vmcnt(7)
	v_mul_f32_e32 v75, v74, v74
	v_pk_add_f32 v[6:7], v[6:7], v[74:75]
	s_waitcnt vmcnt(6)
	v_mul_f32_e32 v93, v92, v92
	v_pk_add_f32 v[6:7], v[6:7], v[92:93]
	s_waitcnt vmcnt(5)
	v_mul_f32_e32 v95, v94, v94
	v_pk_add_f32 v[6:7], v[6:7], v[94:95]
	s_waitcnt vmcnt(4)
	v_mul_f32_e32 v97, v96, v96
	v_pk_add_f32 v[6:7], v[6:7], v[96:97]
	s_waitcnt vmcnt(3)
	v_mul_f32_e32 v99, v98, v98
	v_pk_add_f32 v[6:7], v[6:7], v[98:99]
	s_waitcnt vmcnt(2)
	v_mul_f32_e32 v91, v90, v90
	v_pk_add_f32 v[6:7], v[6:7], v[90:91]
	s_waitcnt vmcnt(1)
	v_mul_f32_e32 v101, v100, v100
	v_pk_add_f32 v[6:7], v[6:7], v[100:101]
	s_waitcnt vmcnt(0)
	v_mul_f32_e32 v67, v66, v66
	v_pk_add_f32 v[6:7], v[6:7], v[66:67]
	v_lshlrev_b32_e32 v5, 2, v0
	s_movk_i32 s4, 0x780
	v_and_or_b32 v9, v5, s4, v4
	v_add_u32_e32 v9, 0x80, v9
	v_cmp_gt_u32_e32 vcc, 32, v0
	ds_write2st64_b32 v9, v7, v6 offset0:128 offset1:136
	s_waitcnt lgkmcnt(0)
	s_barrier
	s_and_saveexec_b64 s[18:19], vcc
	s_cbranch_execz .LBB0_5
	v_add_u32_e32 v9, 0x8800, v5
	ds_read2_b32 v[6:7], v9 offset0:32 offset1:64
	v_add_u32_e32 v18, 0x8000, v5
	ds_read2_b32 v[10:11], v18 offset0:32 offset1:64
	ds_read2_b32 v[12:13], v9 offset0:96 offset1:128
	ds_read2_b32 v[14:15], v18 offset0:96 offset1:128
	ds_read2_b32 v[16:17], v9 offset0:160 offset1:192
	ds_read2_b32 v[18:19], v18 offset0:160 offset1:192
	s_waitcnt lgkmcnt(4)
	v_mov_b32_e32 v20, v10
	v_add_u32_e32 v9, 0x8a00, v5
	v_mov_b32_e32 v21, v6
	v_pk_add_f32 v[20:21], v[20:21], 0 op_sel_hi:[1,0]
	v_mov_b32_e32 v6, v11
	v_pk_add_f32 v[6:7], v[20:21], v[6:7]
	s_waitcnt lgkmcnt(2)
	v_mov_b32_e32 v10, v14
	v_mov_b32_e32 v11, v12
	v_pk_add_f32 v[6:7], v[6:7], v[10:11]
	v_mov_b32_e32 v12, v15
	v_pk_add_f32 v[6:7], v[6:7], v[12:13]
	s_waitcnt lgkmcnt(0)
	v_mov_b32_e32 v10, v18
	v_mov_b32_e32 v11, v16
	v_pk_add_f32 v[6:7], v[6:7], v[10:11]
	ds_read2_b32 v[10:11], v9 offset0:96 offset1:128
	v_add_u32_e32 v9, 0x8200, v5
	ds_read2_b32 v[12:13], v9 offset0:96 offset1:128
	v_add_u32_e32 v9, 0x8c00, v5
	ds_read2_b32 v[14:15], v9 offset0:32 offset1:64
	v_add_u32_e32 v16, 0x8400, v5
	ds_read2_b32 v[20:21], v16 offset0:32 offset1:64
	ds_read2_b32 v[22:23], v9 offset0:96 offset1:128
	ds_read2_b32 v[24:25], v16 offset0:96 offset1:128
	ds_read2_b32 v[26:27], v9 offset0:160 offset1:192
	ds_read2_b32 v[28:29], v16 offset0:160 offset1:192
	v_mov_b32_e32 v16, v19
	v_pk_add_f32 v[6:7], v[6:7], v[16:17]
	s_waitcnt lgkmcnt(6)
	v_mov_b32_e32 v16, v12
	v_mov_b32_e32 v17, v10
	v_add_u32_e32 v9, 0x8e00, v5
	v_pk_add_f32 v[6:7], v[6:7], v[16:17]
	v_mov_b32_e32 v10, v13
	ds_read2_b32 v[30:31], v9 offset0:96 offset1:128
	v_add_u32_e32 v9, 0x8600, v5
	v_pk_add_f32 v[6:7], v[6:7], v[10:11]
	s_waitcnt lgkmcnt(5)
	v_mov_b32_e32 v10, v20
	v_mov_b32_e32 v11, v14
	ds_read2_b32 v[32:33], v9 offset0:96 offset1:128
	v_pk_add_f32 v[6:7], v[6:7], v[10:11]
	v_mov_b32_e32 v14, v21
	v_pk_add_f32 v[6:7], v[6:7], v[14:15]
	s_waitcnt lgkmcnt(4)
	v_mov_b32_e32 v10, v24
	v_mov_b32_e32 v11, v22
	v_pk_add_f32 v[6:7], v[6:7], v[10:11]
	v_mov_b32_e32 v22, v25
	v_pk_add_f32 v[6:7], v[6:7], v[22:23]
	s_waitcnt lgkmcnt(2)
	v_mov_b32_e32 v10, v28
	v_mov_b32_e32 v11, v26
	v_pk_add_f32 v[6:7], v[6:7], v[10:11]
	v_mov_b32_e32 v26, v29
	v_pk_add_f32 v[6:7], v[6:7], v[26:27]
	s_waitcnt lgkmcnt(0)
	v_mov_b32_e32 v10, v32
	v_mov_b32_e32 v11, v30
	v_pk_add_f32 v[6:7], v[6:7], v[10:11]
	v_mov_b32_e32 v30, v33
	v_pk_add_f32 v[6:7], v[6:7], v[30:31]
	s_mov_b32 s4, 0x3b000000
	v_pk_mul_f32 v[6:7], v[6:7], s[4:5] op_sel_hi:[1,0]
	s_mov_b32 s4, 0xf800000
	v_fma_f32 v6, -v7, v7, v6
	v_cmp_ngt_f32_e32 vcc, 0, v6
	v_add_u32_e32 v5, 0x9000, v5
	s_nop 0
	v_cndmask_b32_e32 v6, 0, v6, vcc
	v_add_f32_e32 v6, 0x3727c5ac, v6
	v_mul_f32_e32 v9, 0x4f800000, v6
	v_cmp_gt_f32_e32 vcc, s4, v6
	s_nop 1
	v_cndmask_b32_e32 v6, v6, v9, vcc
	v_sqrt_f32_e32 v9, v6
	s_nop 0
	v_add_u32_e32 v10, -1, v9
	v_fma_f32 v11, -v10, v9, v6
	v_cmp_ge_f32_e64 s[4:5], 0, v11
	v_add_u32_e32 v11, 1, v9
	s_nop 0
	v_cndmask_b32_e64 v10, v9, v10, s[4:5]
	v_fma_f32 v9, -v11, v9, v6
	v_cmp_lt_f32_e64 s[4:5], 0, v9
	s_nop 1
	v_cndmask_b32_e64 v9, v10, v11, s[4:5]
	v_mul_f32_e32 v10, 0x37800000, v9
	v_cndmask_b32_e32 v9, v9, v10, vcc
	v_mov_b32_e32 v10, 0x260
	v_cmp_class_f32_e32 vcc, v6, v10
	s_nop 1
	v_cndmask_b32_e32 v6, v9, v6, vcc
	v_div_scale_f32 v9, s[4:5], v6, v6, 1.0
	v_rcp_f32_e32 v10, v9
	s_lshl_b32 s4, s16, 12
	s_or_b32 s4, s4, s3
	v_fma_f32 v11, -v9, v10, 1.0
	v_fmac_f32_e32 v10, v11, v10
	v_div_scale_f32 v11, vcc, 1.0, v6, 1.0
	v_mul_f32_e32 v12, v11, v10
	v_fma_f32 v13, -v9, v12, v11
	v_fmac_f32_e32 v12, v13, v10
	v_fma_f32 v9, -v9, v12, v11
	v_div_fmas_f32 v9, v9, v10, v12
	v_or_b32_e32 v10, s4, v0
	v_mov_b32_e32 v11, 0
	v_lshlrev_b64 v[10:11], 2, v[10:11]
	v_div_fixup_f32 v9, v9, v6, 1.0
	v_lshl_add_u64 v[12:13], s[12:13], 0, v[10:11]
	ds_write2_b32 v5, v7, v9 offset0:32 offset1:64
	global_store_dword v[12:13], v7, off
	v_lshl_add_u64 v[6:7], s[14:15], 0, v[10:11]
	global_store_dword v[6:7], v9, off

	.amdhsa_kernel _Z4k_lnPKfS0_S0_PDF16_PfS2_7CvtArgs
		.amdhsa_group_segment_fixed_size 37248
		.amdhsa_private_segment_fixed_size 0
		.amdhsa_kernarg_size 152
		.amdhsa_user_sgpr_count 2
		.amdhsa_user_sgpr_dispatch_ptr 0
		.amdhsa_user_sgpr_queue_ptr 0
		.amdhsa_user_sgpr_kernarg_segment_ptr 1
		.amdhsa_user_sgpr_dispatch_id 0
		.amdhsa_user_sgpr_kernarg_preload_length 0
		.amdhsa_user_sgpr_kernarg_preload_offset 0
		.amdhsa_user_sgpr_private_segment_size 0
		.amdhsa_uses_dynamic_stack 0
		.amdhsa_enable_private_segment 0
		.amdhsa_system_sgpr_workgroup_id_x 1
		.amdhsa_system_sgpr_workgroup_id_y 0
		.amdhsa_system_sgpr_workgroup_id_z 0
		.amdhsa_system_sgpr_workgroup_info 0
		.amdhsa_system_vgpr_workitem_id 0
		.amdhsa_next_free_vgpr 102
		.amdhsa_next_free_sgpr 34
		.amdhsa_accum_offset 104
		.amdhsa_reserve_vcc 1
		.amdhsa_float_round_mode_32 0
		.amdhsa_float_round_mode_16_64 0
		.amdhsa_float_denorm_mode_32 3
		.amdhsa_float_denorm_mode_16_64 3
		.amdhsa_dx10_clamp 1
		.amdhsa_ieee_mode 1
		.amdhsa_fp16_overflow 0
		.amdhsa_tg_split 0
		.amdhsa_exception_fp_ieee_invalid_op 0
		.amdhsa_exception_fp_denorm_src 0
		.amdhsa_exception_fp_ieee_div_zero 0
		.amdhsa_exception_fp_ieee_overflow 0
		.amdhsa_exception_fp_ieee_underflow 0
		.amdhsa_exception_fp_ieee_inexact 0
		.amdhsa_exception_int_div_zero 0
	.end_amdhsa_kernel

amdhsa.kernels:
  - .agpr_count:     0
    .args:
      - .actual_access:  read_only
        .address_space:  global
        .offset:         0
        .size:           8
        .value_kind:     global_buffer
      - .actual_access:  read_only
        .address_space:  global
        .offset:         8
        .size:           8
        .value_kind:     global_buffer
      - .actual_access:  read_only
        .address_space:  global
        .offset:         16
        .size:           8
        .value_kind:     global_buffer
      - .actual_access:  write_only
        .address_space:  global
        .offset:         24
        .size:           8
        .value_kind:     global_buffer
      - .actual_access:  write_only
        .address_space:  global
        .offset:         32
        .size:           8
        .value_kind:     global_buffer
      - .actual_access:  write_only
        .address_space:  global
        .offset:         40
        .size:           8
        .value_kind:     global_buffer
      - .offset:         48
        .size:           104
        .value_kind:     by_value
    .group_segment_fixed_size: 37248
    .kernarg_segment_align: 8
    .kernarg_segment_size: 152
    .language:       OpenCL C
    .language_version:
      - 2
      - 0
    .max_flat_workgroup_size: 512
    .name:           _Z4k_lnPKfS0_S0_PDF16_PfS2_7CvtArgs
    .private_segment_fixed_size: 0
    .sgpr_count:     40
    .sgpr_spill_count: 0
    .symbol:         _Z4k_lnPKfS0_S0_PDF16_PfS2_7CvtArgs.kd
    .uniform_work_group_size: 1
    .uses_dynamic_stack: false
    .vgpr_count:     102
    .vgpr_spill_count: 0
    .wavefront_size: 64
  - .agpr_count:     36
    .args:
      - .actual_access:  read_only
        .address_space:  global
        .offset:         0
        .size:           8
        .value_kind:     global_buffer
      - .actual_access:  read_only
        .address_space:  global
        .offset:         8
        .size:           8
        .value_kind:     global_buffer
      - .actual_access:  read_only
        .address_space:  global
        .offset:         16
        .size:           8
        .value_kind:     global_buffer
      - .actual_access:  read_only
        .address_space:  global
        .offset:         24
        .size:           8
        .value_kind:     global_buffer
      - .actual_access:  read_only
        .address_space:  global
        .offset:         32
        .size:           8
        .value_kind:     global_buffer
      - .actual_access:  read_only
        .address_space:  global
        .offset:         40
        .size:           8
        .value_kind:     global_buffer
      - .actual_access:  read_only
        .address_space:  global
        .offset:         48
        .size:           8
        .value_kind:     global_buffer
      - .actual_access:  read_only
        .address_space:  global
        .offset:         56
        .size:           8
        .value_kind:     global_buffer
      - .actual_access:  write_only
        .address_space:  global
        .offset:         64
        .size:           8
        .value_kind:     global_buffer
      - .actual_access:  write_only
        .address_space:  global
        .offset:         72
        .size:           8
        .value_kind:     global_buffer
      - .actual_access:  write_only
        .address_space:  global
        .offset:         80
        .size:           8
        .value_kind:     global_buffer
      - .actual_access:  write_only
        .address_space:  global
        .offset:         88
        .size:           8
        .value_kind:     global_buffer
      - .actual_access:  write_only
        .address_space:  global
        .offset:         96
        .size:           8
        .value_kind:     global_buffer
    .group_segment_fixed_size: 77312
    .kernarg_segment_align: 8
    .kernarg_segment_size: 104
    .language:       OpenCL C
    .language_version:
      - 2
      - 0
    .max_flat_workgroup_size: 256
    .name:           _Z7k_frontPKDF16_S0_PKfS2_S0_S2_S2_S2_PjPfS4_S4_S4_
    .private_segment_fixed_size: 0
    .sgpr_count:     25
    .sgpr_spill_count: 0
    .symbol:         _Z7k_frontPKDF16_S0_PKfS2_S0_S2_S2_S2_PjPfS4_S4_S4_.kd
    .uniform_work_group_size: 1
    .uses_dynamic_stack: false
    .vgpr_count:     204
    .vgpr_spill_count: 0
    .wavefront_size: 64
  - .agpr_count:     0
    .args:
      - .actual_access:  read_only
        .address_space:  global
        .offset:         0
        .size:           8
        .value_kind:     global_buffer
      - .address_space:  global
        .offset:         8
        .size:           8
        .value_kind:     global_buffer
      - .actual_access:  read_only
        .address_space:  global
        .offset:         16
        .size:           8
        .value_kind:     global_buffer
    .group_segment_fixed_size: 0
    .kernarg_segment_align: 8
    .kernarg_segment_size: 24
    .language:       OpenCL C
    .language_version:
      - 2
      - 0
    .max_flat_workgroup_size: 64
    .name:           _Z7k_scan2PKfPfS0_
    .private_segment_fixed_size: 0
    .sgpr_count:     48
    .sgpr_spill_count: 0
    .symbol:         _Z7k_scan2PKfPfS0_.kd
    .uniform_work_group_size: 1
    .uses_dynamic_stack: false
    .vgpr_count:     150
    .vgpr_spill_count: 0
    .wavefront_size: 64
  - .agpr_count:     0
    .args:
      - .actual_access:  read_only
        .address_space:  global
        .offset:         0
        .size:           8
        .value_kind:     global_buffer
      - .actual_access:  read_only
        .address_space:  global
        .offset:         8
        .size:           8
        .value_kind:     global_buffer
      - .actual_access:  read_only
        .address_space:  global
        .offset:         16
        .size:           8
        .value_kind:     global_buffer
      - .actual_access:  read_only
        .address_space:  global
        .offset:         24
        .size:           8
        .value_kind:     global_buffer
      - .actual_access:  read_only
        .address_space:  global
        .offset:         32
        .size:           8
        .value_kind:     global_buffer
      - .actual_access:  read_only
        .address_space:  global
        .offset:         40
        .size:           8
        .value_kind:     global_buffer
      - .actual_access:  read_only
        .address_space:  global
        .offset:         48
        .size:           8
        .value_kind:     global_buffer
      - .actual_access:  read_only
        .address_space:  global
        .offset:         56
        .size:           8
        .value_kind:     global_buffer
      - .actual_access:  read_only
        .address_space:  global
        .offset:         64
        .size:           8
        .value_kind:     global_buffer
      - .offset:         72
        .size:           72
        .value_kind:     by_value
    .group_segment_fixed_size: 60416
    .kernarg_segment_align: 8
    .kernarg_segment_size: 144
    .language:       OpenCL C
    .language_version:
      - 2
      - 0
    .max_flat_workgroup_size: 256
    .name:           _Z7k_scan3PKjPKfS2_S2_S2_S2_PKDF16_S4_S4_7EpiArgs
    .private_segment_fixed_size: 0
    .sgpr_count:     34
    .sgpr_spill_count: 0
    .symbol:         _Z7k_scan3PKjPKfS2_S2_S2_S2_PKDF16_S4_S4_7EpiArgs.kd
    .uniform_work_group_size: 1
    .uses_dynamic_stack: false
    .vgpr_count:     236
    .vgpr_spill_count: 0
    .wavefront_size: 64
  - .agpr_count:     0
    .args:
      - .actual_access:  read_only
        .address_space:  global
        .offset:         0
        .size:           8
        .value_kind:     global_buffer
      - .actual_access:  read_only
        .address_space:  global
        .offset:         8
        .size:           8
        .value_kind:     global_buffer
      - .actual_access:  read_only
        .address_space:  global
        .offset:         16
        .size:           8
        .value_kind:     global_buffer
      - .actual_access:  write_only
        .address_space:  global
        .offset:         24
        .size:           8
        .value_kind:     global_buffer
    .group_segment_fixed_size: 20160
    .kernarg_segment_align: 8
    .kernarg_segment_size: 32
    .language:       OpenCL C
    .language_version:
      - 2
      - 0
    .max_flat_workgroup_size: 256
    .name:           _Z8k_dwconvPKDF16_PKfS2_PDF16_
    .private_segment_fixed_size: 0
    .sgpr_count:     86
    .sgpr_spill_count: 0
    .symbol:         _Z8k_dwconvPKDF16_PKfS2_PDF16_.kd
    .uniform_work_group_size: 1
    .uses_dynamic_stack: false
    .vgpr_count:     65
    .vgpr_spill_count: 0
    .wavefront_size: 64
  - .agpr_count:     0
    .args:
      - .actual_access:  read_only
        .address_space:  global
        .offset:         0
        .size:           8
        .value_kind:     global_buffer
      - .offset:         8
        .size:           72
        .value_kind:     by_value
    .group_segment_fixed_size: 38912
    .kernarg_segment_align: 8
    .kernarg_segment_size: 80
    .language:       OpenCL C
    .language_version:
      - 2
      - 0
    .max_flat_workgroup_size: 256
    .name:           _Z9k_gemm_tlILi2ELb1EEvPKDF16_6TlArgs
    .private_segment_fixed_size: 0
    .sgpr_count:     27
    .sgpr_spill_count: 0
    .symbol:         _Z9k_gemm_tlILi2ELb1EEvPKDF16_6TlArgs.kd
    .uniform_work_group_size: 1
    .uses_dynamic_stack: false
    .vgpr_count:     124
    .vgpr_spill_count: 0
    .wavefront_size: 64
  - .agpr_count:     0
    .args:
      - .actual_access:  read_only
        .address_space:  global
        .offset:         0
        .size:           8
        .value_kind:     global_buffer
      - .offset:         8
        .size:           72
        .value_kind:     by_value
    .group_segment_fixed_size: 34816
    .kernarg_segment_align: 8
    .kernarg_segment_size: 80
    .language:       OpenCL C
    .language_version:
      - 2
      - 0
    .max_flat_workgroup_size: 256
    .name:           _Z9k_gemm_tlILi3ELb0EEvPKDF16_6TlArgs
    .private_segment_fixed_size: 0
    .sgpr_count:     18
    .sgpr_spill_count: 0
    .symbol:         _Z9k_gemm_tlILi3ELb0EEvPKDF16_6TlArgs.kd
    .uniform_work_group_size: 1
    .uses_dynamic_stack: false
    .vgpr_count:     110
    .vgpr_spill_count: 0
    .wavefront_size: 64
